# loop-invariant code motion: the six conv weight vectors loaded once before the row loop (7 loads per row instead of 13)
# speedup vs baseline: 1.0061x; 1.0024x over previous
.LBB0_1891:
	v_readlane_b32 s40, v253, 14
	v_readlane_b32 s1, v252, 37
	v_mov_b32_e32 v4, v0
	v_readlane_b32 s41, v253, 15
	v_mov_b32_e32 v2, s1
	s_waitcnt vmcnt(0)
	s_barrier
	ds_read_b64 v[6:7], v2
	s_cmp_lt_i32 s34, s86
	s_waitcnt lgkmcnt(0)
	v_readfirstlane_b32 s1, v6
	v_readfirstlane_b32 s2, v7
	s_cbranch_scc0 .LBB0_1898
	s_mul_i32 s92, s26, 0x600
	s_lshl_b64 s[6:7], s[92:93], 2
	s_add_u32 s6, s1, s6
	v_lshlrev_b32_e32 v2, 5, v4
	s_addc_u32 s7, s2, s7
	v_and_b32_e32 v2, 0x7e0, v2
	v_lshl_add_u64 v[8:9], s[6:7], 0, v[2:3]
	s_mov_b64 s[2:3], 0x1000
	v_and_b32_e32 v5, 64, v207
	s_ashr_i32 s35, s34, 31
	v_lshl_add_u64 v[10:11], v[8:9], 0, s[2:3]
	v_xor_b32_e32 v2, 16, v207
	v_add_u32_e32 v5, 64, v5
	s_lshl_b64 s[2:3], s[34:35], 12
	v_cmp_lt_i32_e32 vcc, v2, v5
	s_add_u32 s1, s40, s2
	s_addc_u32 s2, s41, s3
	v_cndmask_b32_e32 v2, v207, v2, vcc
	v_lshlrev_b32_e32 v22, 2, v2
	v_xor_b32_e32 v2, 32, v207
	s_add_u32 s36, s1, 0x51200000
	v_cmp_lt_i32_e32 vcc, v2, v5
	s_addc_u32 s37, s2, 0
	s_ashr_i32 s1, s0, 31
	v_cndmask_b32_e32 v2, v207, v2, vcc
	s_lshl_b64 s[38:39], s[0:1], 12
	s_mul_i32 s2, s34, 0xc00
	v_lshlrev_b32_e32 v23, 2, v2
	v_and_b32_e32 v2, 63, v4
	s_mul_hi_i32 s1, s34, 0xc00
	s_add_u32 s40, s40, s2
	v_lshlrev_b32_e32 v2, 4, v2
	s_addc_u32 s41, s41, s1
	global_load_dwordx4 v[80:83], v[8:9], off offset:16
	global_load_dwordx4 v[84:87], v[8:9], off
	global_load_dwordx4 v[88:91], v[10:11], off offset:16
	global_load_dwordx4 v[92:95], v[10:11], off
	global_load_dwordx4 v[96:99], v[8:9], off offset:2048
	global_load_dwordx4 v[100:103], v[8:9], off offset:2064
	s_branch .LBB0_1894

.LBB0_1894:
	v_lshl_add_u64 v[20:21], s[40:41], 0, v[2:3]
	v_add_co_u32_e32 v4, vcc, 0x44600000, v20
	s_cmpk_lt_i32 s34, 0x4000
	s_nop 0
	v_addc_co_u32_e32 v5, vcc, 0, v21, vcc
	global_load_dwordx4 v[12:15], v[4:5], off offset:1024
	global_load_dwordx4 v[16:19], v[4:5], off offset:2048
	s_nop 0
	global_load_dwordx4 v[4:7], v[4:5], off
	v_add_co_u32_e32 v76, vcc, 0x445ff000, v20
	s_nop 1
	v_addc_co_u32_e32 v77, vcc, 0, v21, vcc
	v_add_co_u32_e32 v78, vcc, 0x44601000, v20
	s_nop 1
	v_addc_co_u32_e32 v79, vcc, 0, v21, vcc
	global_load_dwordx4 v[44:47], v[76:77], off offset:2048
	global_load_dwordx4 v[48:51], v[76:77], off offset:3072
	global_load_dwordx4 v[60:63], v[78:79], off
	global_load_dwordx4 v[64:67], v[78:79], off offset:1024
	s_movk_i32 s1, 0xfff
	s_cselect_b32 s1, s1, 0xff
	s_and_b32 s2, s1, s34
	s_cmp_eq_u32 s2, 0
	s_waitcnt vmcnt(6)
	v_lshlrev_b32_e32 v32, 16, v12
	v_and_b32_e32 v33, 0xffff0000, v12
	s_waitcnt vmcnt(5)
	v_lshlrev_b32_e32 v34, 16, v16
	v_and_b32_e32 v35, 0xffff0000, v16
	v_lshlrev_b32_e32 v12, 16, v13
	v_and_b32_e32 v13, 0xffff0000, v13
	v_lshlrev_b32_e32 v16, 16, v17
	v_and_b32_e32 v17, 0xffff0000, v17
	v_lshlrev_b32_e32 v36, 16, v14
	v_and_b32_e32 v37, 0xffff0000, v14
	v_lshlrev_b32_e32 v38, 16, v18
	v_and_b32_e32 v39, 0xffff0000, v18
	v_lshlrev_b32_e32 v14, 16, v15
	v_and_b32_e32 v15, 0xffff0000, v15
	v_lshlrev_b32_e32 v18, 16, v19
	v_and_b32_e32 v19, 0xffff0000, v19
	v_pk_mul_f32 v[32:33], v[32:33], v[34:35]
	v_pk_mul_f32 v[16:17], v[12:13], v[16:17]
	v_pk_mul_f32 v[34:35], v[36:37], v[38:39]
	v_pk_mul_f32 v[18:19], v[14:15], v[18:19]
	s_waitcnt vmcnt(5)
v_mov_b32_e32 v24, v96
	v_mov_b32_e32 v25, v97
	v_mov_b32_e32 v26, v98
	v_mov_b32_e32 v27, v99
	v_pk_mul_f32 v[12:13], v[32:33], v[24:25]
	v_pk_mul_f32 v[14:15], v[16:17], v[26:27]
	s_waitcnt vmcnt(5)
v_mov_b32_e32 v28, v100
	v_mov_b32_e32 v29, v101
	v_mov_b32_e32 v30, v102
	v_mov_b32_e32 v31, v103
	v_pk_mul_f32 v[16:17], v[34:35], v[28:29]
	v_pk_mul_f32 v[18:19], v[18:19], v[30:31]
	s_cbranch_scc1 .LBB0_1896
	s_nop 1
	s_nop 0
	s_nop 0
	s_waitcnt vmcnt(3)
	v_mov_b32_e32 v24, v44
	v_mov_b32_e32 v25, v45
	v_mov_b32_e32 v26, v46
	v_mov_b32_e32 v27, v47
	v_lshlrev_b32_e32 v40, 16, v24
	v_and_b32_e32 v41, 0xffff0000, v24
	s_waitcnt vmcnt(2)
	v_mov_b32_e32 v28, v48
	v_mov_b32_e32 v29, v49
	v_mov_b32_e32 v30, v50
	v_mov_b32_e32 v31, v51
	v_lshlrev_b32_e32 v42, 16, v28
	v_and_b32_e32 v43, 0xffff0000, v28
	v_lshlrev_b32_e32 v24, 16, v25
	v_and_b32_e32 v25, 0xffff0000, v25
	v_lshlrev_b32_e32 v28, 16, v29
	v_and_b32_e32 v29, 0xffff0000, v29
	v_pk_mul_f32 v[24:25], v[24:25], v[28:29]
	v_lshlrev_b32_e32 v28, 16, v30
	s_waitcnt vmcnt(2)
	v_mov_b32_e32 v32, v80
	v_mov_b32_e32 v33, v81
	v_mov_b32_e32 v34, v82
	v_mov_b32_e32 v35, v83
	v_mov_b32_e32 v36, v84
	v_mov_b32_e32 v37, v85
	v_mov_b32_e32 v38, v86
	v_mov_b32_e32 v39, v87
	v_pk_fma_f32 v[14:15], v[24:25], v[38:39], v[14:15]
	v_lshlrev_b32_e32 v24, 16, v26
	v_and_b32_e32 v25, 0xffff0000, v26
	v_and_b32_e32 v29, 0xffff0000, v30
	v_pk_mul_f32 v[24:25], v[24:25], v[28:29]
	v_lshlrev_b32_e32 v26, 16, v31
	v_pk_fma_f32 v[16:17], v[24:25], v[32:33], v[16:17]
	v_lshlrev_b32_e32 v24, 16, v27
	v_and_b32_e32 v25, 0xffff0000, v27
	v_and_b32_e32 v27, 0xffff0000, v31
	v_pk_mul_f32 v[40:41], v[40:41], v[42:43]
	v_pk_mul_f32 v[24:25], v[24:25], v[26:27]
	v_pk_fma_f32 v[12:13], v[40:41], v[36:37], v[12:13]
	v_pk_fma_f32 v[18:19], v[24:25], v[34:35], v[18:19]
.LBB0_1896:
	s_cmp_eq_u32 s2, s1
	s_cbranch_scc1 .LBB0_1893
	s_nop 1
	s_waitcnt vmcnt(1)
	v_mov_b32_e32 v24, v60
	v_mov_b32_e32 v25, v61
	v_mov_b32_e32 v26, v62
	v_mov_b32_e32 v27, v63
	v_lshlrev_b32_e32 v20, 16, v24
	v_and_b32_e32 v21, 0xffff0000, v24
	s_waitcnt vmcnt(0)
	v_mov_b32_e32 v28, v64
	v_mov_b32_e32 v29, v65
	v_mov_b32_e32 v30, v66
	v_mov_b32_e32 v31, v67
	v_lshlrev_b32_e32 v40, 16, v28
	v_and_b32_e32 v41, 0xffff0000, v28
	v_pk_mul_f32 v[20:21], v[20:21], v[40:41]
	v_lshlrev_b32_e32 v24, 16, v29
	s_waitcnt vmcnt(0)
	v_mov_b32_e32 v32, v88
	v_mov_b32_e32 v33, v89
	v_mov_b32_e32 v34, v90
	v_mov_b32_e32 v35, v91
	v_mov_b32_e32 v36, v92
	v_mov_b32_e32 v37, v93
	v_mov_b32_e32 v38, v94
	v_mov_b32_e32 v39, v95
	v_pk_fma_f32 v[12:13], v[20:21], v[36:37], v[12:13]
	v_lshlrev_b32_e32 v20, 16, v25
	v_and_b32_e32 v21, 0xffff0000, v25
	v_and_b32_e32 v25, 0xffff0000, v29
	v_pk_mul_f32 v[20:21], v[20:21], v[24:25]
	v_lshlrev_b32_e32 v24, 16, v30
	v_pk_fma_f32 v[14:15], v[20:21], v[38:39], v[14:15]
	v_lshlrev_b32_e32 v20, 16, v26
	v_and_b32_e32 v21, 0xffff0000, v26
	v_and_b32_e32 v25, 0xffff0000, v30
	v_pk_mul_f32 v[20:21], v[20:21], v[24:25]
	v_lshlrev_b32_e32 v24, 16, v31
	v_pk_fma_f32 v[16:17], v[20:21], v[32:33], v[16:17]
	v_lshlrev_b32_e32 v20, 16, v27
	v_and_b32_e32 v21, 0xffff0000, v27
	v_and_b32_e32 v25, 0xffff0000, v31
	v_pk_mul_f32 v[20:21], v[20:21], v[24:25]
	s_nop 0
	v_pk_fma_f32 v[18:19], v[20:21], v[34:35], v[18:19]
	s_branch .LBB0_1893
